# v59 + gate/up epilogue biases fetched one unit ahead and parked in LDS (no vmcnt(0) in the epilogue)
# baseline (speedup 1.0000x reference)
.LBB0_801:
	v_and_b32_e32 v5, 15, v4
	s_add_i32 s0, 0, 0x21000
	v_or_b32_e32 v6, s53, v5
	v_lshl_add_u32 v253, v4, 4, s0
	v_and_b32_e32 v7, 48, v4
	v_lshlrev_b32_e32 v8, 6, v6
	s_movk_i32 s0, 0x3c0
	v_and_or_b32 v8, v8, s0, v7
	v_lshlrev_b32_e32 v4, 2, v4
	s_add_u32 s0, s18, 0x80
	v_lshl_or_b32 v5, v5, 6, v7
	v_and_b32_e32 v4, 32, v4
	s_addc_u32 s1, s19, 0
	v_bitop3_b32 v158, v5, s56, v4 bitop3:0xde
	s_waitcnt vmcnt(2)
	s_barrier
	s_add_i32 m0, s7, 0x18000
	v_lshl_add_u64 v[4:5], s[0:1], 0, v[140:141]
	global_load_lds_dwordx4 v[4:5], off
	s_add_i32 m0, s7, 0x1a000
	v_lshl_add_u64 v[4:5], s[0:1], 0, v[142:143]
	s_add_u32 s0, s90, 0x12800080
	s_addc_u32 s1, s91, 0
	s_add_i32 s60, s7, 0x8000
	global_load_lds_dwordx4 v[4:5], off
	s_mov_b32 m0, s60
	v_lshl_add_u64 v[4:5], s[0:1], 0, v[0:1]
	s_add_i32 s61, s7, 0xa000
	global_load_lds_dwordx4 v[4:5], off
	v_lshl_add_u64 v[4:5], s[0:1], 0, v[144:145]
	s_add_u32 s0, s18, 0x40080
	s_mov_b32 m0, s61
	s_addc_u32 s1, s19, 0
	global_load_lds_dwordx4 v[4:5], off
	s_add_i32 m0, s7, 0x1c000
	v_lshl_add_u64 v[4:5], s[0:1], 0, v[140:141]
	global_load_lds_dwordx4 v[4:5], off
	v_lshl_add_u64 v[4:5], s[0:1], 0, v[142:143]
	s_add_i32 m0, s7, 0x1e000
	v_lshlrev_b32_e32 v6, 2, v6
	global_load_lds_dwordx4 v[4:5], off
	v_and_b32_e32 v6, 32, v6
	s_waitcnt vmcnt(6)
	v_readlane_b32 s0, v255, 25
	v_bitop3_b32 v6, v8, s55, v6 bitop3:0xde
	s_cmpk_lt_u32 s0, 0x100
	s_cselect_b64 s[22:23], -1, 0
	s_add_i32 s62, 0, 0x10000
	s_add_i32 s63, 0, 0x14000
	v_add_u32_e32 v143, 0, v6
	v_mov_b32_e32 v145, 0x7f7f7f7f
	s_mov_b32 s24, 0x3c800000
	s_mov_b32 s64, 0xc0c00000
	v_mov_b32_e32 v159, 0x41000000
	v_mov_b32_e32 v4, v141
	v_mov_b32_e32 v5, v141
	v_mov_b32_e32 v6, v141
	v_mov_b32_e32 v7, v141
	v_mov_b32_e32 v8, v141
	v_mov_b32_e32 v9, v141
	v_mov_b32_e32 v10, v141
	v_mov_b32_e32 v11, v141
	v_mov_b32_e32 v12, v141
	v_mov_b32_e32 v13, v141
	v_mov_b32_e32 v14, v141
	v_mov_b32_e32 v15, v141
	v_mov_b32_e32 v16, v141
	v_mov_b32_e32 v17, v141
	v_mov_b32_e32 v18, v141
	v_mov_b32_e32 v19, v141
	v_mov_b32_e32 v20, v141
	v_mov_b32_e32 v21, v141
	v_mov_b32_e32 v22, v141
	v_mov_b32_e32 v23, v141
	v_mov_b32_e32 v24, v141
	v_mov_b32_e32 v25, v141
	v_mov_b32_e32 v26, v141
	v_mov_b32_e32 v27, v141
	v_mov_b32_e32 v232, v141
	v_mov_b32_e32 v233, v141
	v_mov_b32_e32 v234, v141
	v_mov_b32_e32 v235, v141
	v_mov_b32_e32 v32, v141
	v_mov_b32_e32 v33, v141
	v_mov_b32_e32 v34, v141
	v_mov_b32_e32 v35, v141
	v_mov_b32_e32 v36, v141
	v_mov_b32_e32 v37, v141
	v_mov_b32_e32 v38, v141
	v_mov_b32_e32 v39, v141
	v_mov_b32_e32 v40, v141
	v_mov_b32_e32 v41, v141
	v_mov_b32_e32 v42, v141
	v_mov_b32_e32 v43, v141
	v_mov_b32_e32 v44, v141
	v_mov_b32_e32 v45, v141
	v_mov_b32_e32 v46, v141
	v_mov_b32_e32 v47, v141
	v_mov_b32_e32 v48, v141
	v_mov_b32_e32 v49, v141
	v_mov_b32_e32 v50, v141
	v_mov_b32_e32 v51, v141
	v_mov_b32_e32 v52, v141
	v_mov_b32_e32 v53, v141
	v_mov_b32_e32 v54, v141
	v_mov_b32_e32 v55, v141
	v_mov_b32_e32 v56, v141
	v_mov_b32_e32 v57, v141
	v_mov_b32_e32 v58, v141
	v_mov_b32_e32 v59, v141
	v_mov_b32_e32 v60, v141
	v_mov_b32_e32 v61, v141
	v_mov_b32_e32 v62, v141
	v_mov_b32_e32 v63, v141
	v_mov_b32_e32 v64, v141
	v_mov_b32_e32 v65, v141
	v_mov_b32_e32 v66, v141
	v_mov_b32_e32 v67, v141
	v_mov_b32_e32 v28, v141
	v_mov_b32_e32 v29, v141
	v_mov_b32_e32 v30, v141
	v_mov_b32_e32 v31, v141
	v_mov_b32_e32 v72, v141
	v_mov_b32_e32 v73, v141
	v_mov_b32_e32 v74, v141
	v_mov_b32_e32 v75, v141
	v_mov_b32_e32 v76, v141
	v_mov_b32_e32 v77, v141
	v_mov_b32_e32 v78, v141
	v_mov_b32_e32 v79, v141
	v_mov_b32_e32 v80, v141
	v_mov_b32_e32 v81, v141
	v_mov_b32_e32 v82, v141
	v_mov_b32_e32 v83, v141
	v_mov_b32_e32 v84, v141
	v_mov_b32_e32 v85, v141
	v_mov_b32_e32 v86, v141
	v_mov_b32_e32 v87, v141
	v_mov_b32_e32 v88, v141
	v_mov_b32_e32 v89, v141
	v_mov_b32_e32 v90, v141
	v_mov_b32_e32 v91, v141
	v_mov_b32_e32 v92, v141
	v_mov_b32_e32 v93, v141
	v_mov_b32_e32 v94, v141
	v_mov_b32_e32 v95, v141
	v_mov_b32_e32 v96, v141
	v_mov_b32_e32 v97, v141
	v_mov_b32_e32 v98, v141
	v_mov_b32_e32 v99, v141
	v_mov_b32_e32 v100, v141
	v_mov_b32_e32 v101, v141
	v_mov_b32_e32 v102, v141
	v_mov_b32_e32 v103, v141
	v_mov_b32_e32 v104, v141
	v_mov_b32_e32 v105, v141
	v_mov_b32_e32 v106, v141
	v_mov_b32_e32 v107, v141
	v_mov_b32_e32 v108, v141
	v_mov_b32_e32 v109, v141
	v_mov_b32_e32 v110, v141
	v_mov_b32_e32 v111, v141
	v_mov_b32_e32 v112, v141
	v_mov_b32_e32 v113, v141
	v_mov_b32_e32 v114, v141
	v_mov_b32_e32 v115, v141
	v_mov_b32_e32 v116, v141
	v_mov_b32_e32 v117, v141
	v_mov_b32_e32 v118, v141
	v_mov_b32_e32 v119, v141
	v_mov_b32_e32 v120, v141
	v_mov_b32_e32 v121, v141
	v_mov_b32_e32 v122, v141
	v_mov_b32_e32 v123, v141
	v_mov_b32_e32 v124, v141
	v_mov_b32_e32 v125, v141
	v_mov_b32_e32 v126, v141
	v_mov_b32_e32 v127, v141
	v_mov_b32_e32 v128, v141
	v_mov_b32_e32 v129, v141
	v_mov_b32_e32 v130, v141
	v_mov_b32_e32 v131, v141
	s_barrier
	v_mbcnt_lo_u32_b32 v200, -1, 0
	v_mbcnt_hi_u32_b32 v200, -1, v200
	v_lshrrev_b32_e32 v200, 4, v200
	v_readlane_b32 s98, v255, 35
	v_readlane_b32 s99, v255, 36
	v_readlane_b32 s100, v255, 39
	v_readlane_b32 s101, v255, 40
	s_lshl_b32 vcc_lo, s4, 13
	s_add_u32 s98, s98, vcc_lo
	s_addc_u32 s99, s99, 0
	s_add_u32 s100, s100, vcc_lo
	s_addc_u32 s101, s101, 0
	s_lshl_b32 vcc_lo, s6, 7
	s_or_b32 vcc_lo, vcc_lo, s54
	v_lshl_add_u32 v201, v200, 3, vcc_lo
	v_lshlrev_b32_e32 v201, 2, v201
	global_load_dwordx4 v[184:187], v201, s[98:99]
	global_load_dwordx4 v[188:191], v201, s[98:99] offset:16
	global_load_dwordx4 v[192:195], v201, s[100:101]
	global_load_dwordx4 v[196:199], v201, s[100:101] offset:16
	v_lshl_add_u32 v204, v200, 3, s54
	v_lshlrev_b32_e32 v204, 2, v204
	s_and_b32 vcc_lo, s59, 1
	s_lshl_b32 vcc_lo, vcc_lo, 10
	s_add_u32 vcc_lo, vcc_lo, 0x26800
	v_add_u32_e32 v204, vcc_lo, v204
	s_waitcnt vmcnt(0)
	ds_write_b128 v204, v[184:187]
	ds_write_b128 v204, v[188:191] offset:16
	ds_write_b128 v204, v[192:195] offset:512
	ds_write_b128 v204, v[196:199] offset:528
	s_branch .LBB0_804

.LBB0_886:
	v_and_b32_e32 v5, 15, v4
	s_add_i32 s0, 0, 0x21000
	v_or_b32_e32 v6, s53, v5
	v_lshl_add_u32 v253, v4, 4, s0
	v_and_b32_e32 v7, 48, v4
	v_lshlrev_b32_e32 v8, 6, v6
	s_movk_i32 s0, 0x3c0
	v_and_or_b32 v8, v8, s0, v7
	v_lshlrev_b32_e32 v4, 2, v4
	s_add_u32 s0, s18, 0x80
	v_lshl_or_b32 v5, v5, 6, v7
	v_and_b32_e32 v4, 32, v4
	s_addc_u32 s1, s19, 0
	v_bitop3_b32 v158, v5, s56, v4 bitop3:0xde
	s_waitcnt vmcnt(2)
	s_barrier
	s_add_i32 m0, s7, 0x18000
	v_lshl_add_u64 v[4:5], s[0:1], 0, v[140:141]
	v_lshlrev_b32_e32 v6, 2, v6
	global_load_lds_dwordx4 v[4:5], off
	s_add_i32 m0, s7, 0x1a000
	v_and_b32_e32 v6, 32, v6
	v_lshl_add_u64 v[4:5], s[0:1], 0, v[142:143]
	s_add_u32 s0, s90, 0x12800080
	v_bitop3_b32 v6, v8, s55, v6 bitop3:0xde
	s_addc_u32 s1, s91, 0
	s_add_i32 s55, s7, 0x8000
	global_load_lds_dwordx4 v[4:5], off
	s_mov_b32 m0, s55
	v_lshl_add_u64 v[4:5], s[0:1], 0, v[0:1]
	s_add_i32 s56, s7, 0xa000
	global_load_lds_dwordx4 v[4:5], off
	v_lshl_add_u64 v[4:5], s[0:1], 0, v[144:145]
	s_add_u32 s0, s18, 0x40080
	s_mov_b32 m0, s56
	s_addc_u32 s1, s19, 0
	global_load_lds_dwordx4 v[4:5], off
	s_add_i32 m0, s7, 0x1c000
	v_lshl_add_u64 v[4:5], s[0:1], 0, v[140:141]
	global_load_lds_dwordx4 v[4:5], off
	v_lshl_add_u64 v[4:5], s[0:1], 0, v[142:143]
	s_add_i32 m0, s7, 0x1e000
	v_readlane_b32 s0, v255, 25
	global_load_lds_dwordx4 v[4:5], off
	s_waitcnt vmcnt(6)
	s_cmpk_lt_u32 s0, 0x100
	s_cselect_b64 s[22:23], -1, 0
	s_add_i32 s57, 0, 0x10000
	s_add_i32 s61, 0, 0x14000
	v_add_u32_e32 v143, 0, v6
	v_mov_b32_e32 v145, 0x7f7f7f7f
	s_mov_b32 s24, 0x3c800000
	s_mov_b32 s62, 0xc0c00000
	s_mov_b32 s63, 0x40000
	v_mov_b32_e32 v159, 0x41000000
	v_mov_b32_e32 v4, v141
	v_mov_b32_e32 v5, v141
	v_mov_b32_e32 v6, v141
	v_mov_b32_e32 v7, v141
	v_mov_b32_e32 v8, v141
	v_mov_b32_e32 v9, v141
	v_mov_b32_e32 v10, v141
	v_mov_b32_e32 v11, v141
	v_mov_b32_e32 v12, v141
	v_mov_b32_e32 v13, v141
	v_mov_b32_e32 v14, v141
	v_mov_b32_e32 v15, v141
	v_mov_b32_e32 v16, v141
	v_mov_b32_e32 v17, v141
	v_mov_b32_e32 v18, v141
	v_mov_b32_e32 v19, v141
	v_mov_b32_e32 v20, v141
	v_mov_b32_e32 v21, v141
	v_mov_b32_e32 v22, v141
	v_mov_b32_e32 v23, v141
	v_mov_b32_e32 v24, v141
	v_mov_b32_e32 v25, v141
	v_mov_b32_e32 v26, v141
	v_mov_b32_e32 v27, v141
	v_mov_b32_e32 v232, v141
	v_mov_b32_e32 v233, v141
	v_mov_b32_e32 v234, v141
	v_mov_b32_e32 v235, v141
	v_mov_b32_e32 v32, v141
	v_mov_b32_e32 v33, v141
	v_mov_b32_e32 v34, v141
	v_mov_b32_e32 v35, v141
	v_mov_b32_e32 v36, v141
	v_mov_b32_e32 v37, v141
	v_mov_b32_e32 v38, v141
	v_mov_b32_e32 v39, v141
	v_mov_b32_e32 v40, v141
	v_mov_b32_e32 v41, v141
	v_mov_b32_e32 v42, v141
	v_mov_b32_e32 v43, v141
	v_mov_b32_e32 v44, v141
	v_mov_b32_e32 v45, v141
	v_mov_b32_e32 v46, v141
	v_mov_b32_e32 v47, v141
	v_mov_b32_e32 v48, v141
	v_mov_b32_e32 v49, v141
	v_mov_b32_e32 v50, v141
	v_mov_b32_e32 v51, v141
	v_mov_b32_e32 v52, v141
	v_mov_b32_e32 v53, v141
	v_mov_b32_e32 v54, v141
	v_mov_b32_e32 v55, v141
	v_mov_b32_e32 v56, v141
	v_mov_b32_e32 v57, v141
	v_mov_b32_e32 v58, v141
	v_mov_b32_e32 v59, v141
	v_mov_b32_e32 v60, v141
	v_mov_b32_e32 v61, v141
	v_mov_b32_e32 v62, v141
	v_mov_b32_e32 v63, v141
	v_mov_b32_e32 v64, v141
	v_mov_b32_e32 v65, v141
	v_mov_b32_e32 v66, v141
	v_mov_b32_e32 v67, v141
	v_mov_b32_e32 v28, v141
	v_mov_b32_e32 v29, v141
	v_mov_b32_e32 v30, v141
	v_mov_b32_e32 v31, v141
	v_mov_b32_e32 v72, v141
	v_mov_b32_e32 v73, v141
	v_mov_b32_e32 v74, v141
	v_mov_b32_e32 v75, v141
	v_mov_b32_e32 v76, v141
	v_mov_b32_e32 v77, v141
	v_mov_b32_e32 v78, v141
	v_mov_b32_e32 v79, v141
	v_mov_b32_e32 v80, v141
	v_mov_b32_e32 v81, v141
	v_mov_b32_e32 v82, v141
	v_mov_b32_e32 v83, v141
	v_mov_b32_e32 v84, v141
	v_mov_b32_e32 v85, v141
	v_mov_b32_e32 v86, v141
	v_mov_b32_e32 v87, v141
	v_mov_b32_e32 v88, v141
	v_mov_b32_e32 v89, v141
	v_mov_b32_e32 v90, v141
	v_mov_b32_e32 v91, v141
	v_mov_b32_e32 v92, v141
	v_mov_b32_e32 v93, v141
	v_mov_b32_e32 v94, v141
	v_mov_b32_e32 v95, v141
	v_mov_b32_e32 v96, v141
	v_mov_b32_e32 v97, v141
	v_mov_b32_e32 v98, v141
	v_mov_b32_e32 v99, v141
	v_mov_b32_e32 v100, v141
	v_mov_b32_e32 v101, v141
	v_mov_b32_e32 v102, v141
	v_mov_b32_e32 v103, v141
	v_mov_b32_e32 v104, v141
	v_mov_b32_e32 v105, v141
	v_mov_b32_e32 v106, v141
	v_mov_b32_e32 v107, v141
	v_mov_b32_e32 v108, v141
	v_mov_b32_e32 v109, v141
	v_mov_b32_e32 v110, v141
	v_mov_b32_e32 v111, v141
	v_mov_b32_e32 v112, v141
	v_mov_b32_e32 v113, v141
	v_mov_b32_e32 v114, v141
	v_mov_b32_e32 v115, v141
	v_mov_b32_e32 v116, v141
	v_mov_b32_e32 v117, v141
	v_mov_b32_e32 v118, v141
	v_mov_b32_e32 v119, v141
	v_mov_b32_e32 v120, v141
	v_mov_b32_e32 v121, v141
	v_mov_b32_e32 v122, v141
	v_mov_b32_e32 v123, v141
	v_mov_b32_e32 v124, v141
	v_mov_b32_e32 v125, v141
	v_mov_b32_e32 v126, v141
	v_mov_b32_e32 v127, v141
	v_mov_b32_e32 v128, v141
	v_mov_b32_e32 v129, v141
	v_mov_b32_e32 v130, v141
	v_mov_b32_e32 v131, v141
	s_barrier
	v_mbcnt_lo_u32_b32 v200, -1, 0
	v_mbcnt_hi_u32_b32 v200, -1, v200
	v_lshrrev_b32_e32 v200, 4, v200
	v_readlane_b32 s98, v255, 35
	v_readlane_b32 s99, v255, 36
	v_readlane_b32 s100, v255, 39
	v_readlane_b32 s101, v255, 40
	s_lshl_b32 vcc_lo, s4, 13
	s_add_u32 s98, s98, vcc_lo
	s_addc_u32 s99, s99, 0
	s_add_u32 s100, s100, vcc_lo
	s_addc_u32 s101, s101, 0
	s_lshl_b32 vcc_lo, s6, 7
	s_or_b32 vcc_lo, vcc_lo, s54
	v_lshl_add_u32 v201, v200, 3, vcc_lo
	v_lshlrev_b32_e32 v201, 2, v201
	global_load_dwordx4 v[184:187], v201, s[98:99]
	global_load_dwordx4 v[188:191], v201, s[98:99] offset:16
	global_load_dwordx4 v[192:195], v201, s[100:101]
	global_load_dwordx4 v[196:199], v201, s[100:101] offset:16
	v_lshl_add_u32 v204, v200, 3, s54
	v_lshlrev_b32_e32 v204, 2, v204
	s_and_b32 vcc_lo, s60, 1
	s_lshl_b32 vcc_lo, vcc_lo, 10
	s_add_u32 vcc_lo, vcc_lo, 0x26800
	v_add_u32_e32 v204, vcc_lo, v204
	s_waitcnt vmcnt(0)
	ds_write_b128 v204, v[184:187]
	ds_write_b128 v204, v[188:191] offset:16
	ds_write_b128 v204, v[192:195] offset:512
	ds_write_b128 v204, v[196:199] offset:528
	s_branch .LBB0_889
